# conv-in-NSA at softmax-segment start; store path computes only the fp8 scale per item (run address decoded at the flush)
# baseline (speedup 1.0000x reference)
; __device__ __forceinline__ unsigned pk4_fp8(float a, float b, float c, float d) { int p = __builtin_amdgcn_cvt_pk_fp8_f32(a, b, 0, false); p = __builtin_amdgcn_cvt_pk_fp8_f32(c, d, p, true); return (unsigned)p; }
; __device__ __forceinline__ void witem_store(const WItem& w, const f32x4 (&v)[16]) {
;     if (!w.valid) return;
;     if (w.f8) {
; #pragma unroll
;         for (int j = 0; j < 4; ++j) { u32x4 o; const float sc = w.scale;
;             o.x = pk4_fp8(v[0][j] * sc, v[1][j] * sc, v[2][j] * sc, v[3][j] * sc); o.y = pk4_fp8(v[4][j] * sc, v[5][j] * sc, v[6][j] * sc, v[7][j] * sc);
;             o.z = pk4_fp8(v[8][j] * sc, v[9][j] * sc, v[10][j] * sc, v[11][j] * sc); o.w = pk4_fp8(v[12][j] * sc, v[13][j] * sc, v[14][j] * sc, v[15][j] * sc);
;             *(u32x4*)(w.dst + (size_t)witem_row(w.kind, w.n + j) * w.K + w.k0) = o; }
; __device__ __forceinline__ void p0_weights(const Args& a, LAS unsigned char* lds) {
;     ...
;         else if ((r -= I_FD) < 16 * I_MG) { const int up = r / (8 * I_MG); r -= up * 8 * I_MG; const int e = r / I_MG; r -= e * I_MG; W = a.in[up ? I_MWU : I_MWG] + (size_t)e * D * DFE; w.K = D; w.N = DFE;
;             w.dst = a.ws + WS_MGU_T + (size_t)e * 2 * DFE * D * (MOE_FP8 ? 1 : 2); w.kind = 2 + up; w.f8 = MOE_FP8; w.scale = F8_WGU; }
;         else { r -= 16 * I_MG; const int e = r / I_MD; r -= e * I_MD; W = a.in[I_MWD] + (size_t)e * DFE * D; w.K = DFE; w.N = D; w.dst = a.ws + WS_MD_T + (size_t)e * D * DFE * (MOE_FP8 ? 1 : 2); w.f8 = MOE_FP8; w.scale = F8_WD; }
.Lcn_wd_n0:
	s_bitcmp1_b32 s25, 31
	s_cbranch_scc0 .Lcn_snone_n0l
	s_and_b32 s12, s25, 0xfffffff
	s_lshr_b32 s12, s12, 2
	s_lshl_b32 s12, s12, 11
	s_add_u32 s12, s12, s100
	s_mov_b32 s13, 0x42000000
	s_cmp_ge_u32 s12, 0xe000
	s_cselect_b32 s13, 0x43000000, s13
	v_mul_f32_e32 v212, s13, v212
	v_mul_f32_e32 v213, s13, v213
	v_mul_f32_e32 v214, s13, v214
	v_mul_f32_e32 v215, s13, v215
	v_mul_f32_e32 v216, s13, v216
	v_mul_f32_e32 v217, s13, v217
	v_mul_f32_e32 v218, s13, v218
	v_mul_f32_e32 v219, s13, v219
	v_mul_f32_e32 v220, s13, v220
	v_mul_f32_e32 v221, s13, v221
	v_mul_f32_e32 v222, s13, v222
	v_mul_f32_e32 v223, s13, v223
	v_mul_f32_e32 v224, s13, v224
	v_mul_f32_e32 v225, s13, v225
	v_mul_f32_e32 v253, s13, v253
	v_mul_f32_e32 v254, s13, v254
	v_cvt_pk_fp8_f32 v212, v212, v216
	v_cvt_pk_fp8_f32 v213, v213, v217
	v_cvt_pk_fp8_f32 v214, v214, v218
	v_cvt_pk_fp8_f32 v215, v215, v219
	v_cvt_pk_fp8_f32 v212, v220, v224 op_sel:[0,0,1]
	v_cvt_pk_fp8_f32 v213, v221, v225 op_sel:[0,0,1]
	v_cvt_pk_fp8_f32 v214, v222, v253 op_sel:[0,0,1]
	v_cvt_pk_fp8_f32 v215, v223, v254 op_sel:[0,0,1]
	s_and_b32 s12, s25, 3
	v_and_b32_e32 v216, 63, v0
	v_and_b32_e32 v217, 7, v216
	v_lshrrev_b32_e32 v216, 3, v216
	v_and_b32_e32 v218, 3, v217
	v_xor_b32_e32 v218, s12, v218
	v_lshlrev_b32_e32 v218, 5, v218
	v_lshl_add_u32 v218, v216, 2, v218
	v_lshl_add_u32 v218, v217, 9, v218
	v_and_b32_e32 v219, 0x1c0, v0
	v_lshl_add_u32 v218, v219, 6, v218
	v_add_u32_e32 v218, 0x1c000, v218
	ds_write_b32 v218, v212 offset:0
	ds_write_b32 v218, v213 offset:128
	ds_write_b32 v218, v214 offset:256
	ds_write_b32 v218, v215 offset:384
	s_mov_b32 s67, s25
	s_mov_b32 s25, 0

; __device__ __forceinline__ unsigned pk4_fp8(float a, float b, float c, float d) { int p = __builtin_amdgcn_cvt_pk_fp8_f32(a, b, 0, false); p = __builtin_amdgcn_cvt_pk_fp8_f32(c, d, p, true); return (unsigned)p; }
; __device__ __forceinline__ void witem_store(const WItem& w, const f32x4 (&v)[16]) {
;     if (!w.valid) return;
;     if (w.f8) {
; #pragma unroll
;         for (int j = 0; j < 4; ++j) { u32x4 o; const float sc = w.scale;
;             o.x = pk4_fp8(v[0][j] * sc, v[1][j] * sc, v[2][j] * sc, v[3][j] * sc); o.y = pk4_fp8(v[4][j] * sc, v[5][j] * sc, v[6][j] * sc, v[7][j] * sc);
;             o.z = pk4_fp8(v[8][j] * sc, v[9][j] * sc, v[10][j] * sc, v[11][j] * sc); o.w = pk4_fp8(v[12][j] * sc, v[13][j] * sc, v[14][j] * sc, v[15][j] * sc);
;             *(u32x4*)(w.dst + (size_t)witem_row(w.kind, w.n + j) * w.K + w.k0) = o; }
; __device__ __forceinline__ void p0_weights(const Args& a, LAS unsigned char* lds) {
;     ...
;         else if ((r -= I_FD) < 16 * I_MG) { const int up = r / (8 * I_MG); r -= up * 8 * I_MG; const int e = r / I_MG; r -= e * I_MG; W = a.in[up ? I_MWU : I_MWG] + (size_t)e * D * DFE; w.K = D; w.N = DFE;
;             w.dst = a.ws + WS_MGU_T + (size_t)e * 2 * DFE * D * (MOE_FP8 ? 1 : 2); w.kind = 2 + up; w.f8 = MOE_FP8; w.scale = F8_WGU; }
;         else { r -= 16 * I_MG; const int e = r / I_MD; r -= e * I_MD; W = a.in[I_MWD] + (size_t)e * DFE * D; w.K = DFE; w.N = D; w.dst = a.ws + WS_MD_T + (size_t)e * D * DFE * (MOE_FP8 ? 1 : 2); w.f8 = MOE_FP8; w.scale = F8_WD; }
.Lcn_exit_n0:
	s_bitcmp1_b32 s25, 31
	s_cbranch_scc0 .Lcn_xnone_n0
	s_waitcnt vmcnt(0)
	s_bitcmp1_b32 s25, 31
	s_cbranch_scc0 .Lcn_snone_n0x
	s_and_b32 s12, s25, 0xfffffff
	s_lshr_b32 s12, s12, 2
	s_lshl_b32 s12, s12, 11
	s_add_u32 s12, s12, s100
	s_mov_b32 s13, 0x42000000
	s_cmp_ge_u32 s12, 0xe000
	s_cselect_b32 s13, 0x43000000, s13
	v_mul_f32_e32 v212, s13, v212
	v_mul_f32_e32 v213, s13, v213
	v_mul_f32_e32 v214, s13, v214
	v_mul_f32_e32 v215, s13, v215
	v_mul_f32_e32 v216, s13, v216
	v_mul_f32_e32 v217, s13, v217
	v_mul_f32_e32 v218, s13, v218
	v_mul_f32_e32 v219, s13, v219
	v_mul_f32_e32 v220, s13, v220
	v_mul_f32_e32 v221, s13, v221
	v_mul_f32_e32 v222, s13, v222
	v_mul_f32_e32 v223, s13, v223
	v_mul_f32_e32 v224, s13, v224
	v_mul_f32_e32 v225, s13, v225
	v_mul_f32_e32 v253, s13, v253
	v_mul_f32_e32 v254, s13, v254
	v_cvt_pk_fp8_f32 v212, v212, v216
	v_cvt_pk_fp8_f32 v213, v213, v217
	v_cvt_pk_fp8_f32 v214, v214, v218
	v_cvt_pk_fp8_f32 v215, v215, v219
	v_cvt_pk_fp8_f32 v212, v220, v224 op_sel:[0,0,1]
	v_cvt_pk_fp8_f32 v213, v221, v225 op_sel:[0,0,1]
	v_cvt_pk_fp8_f32 v214, v222, v253 op_sel:[0,0,1]
	v_cvt_pk_fp8_f32 v215, v223, v254 op_sel:[0,0,1]
	s_and_b32 s12, s25, 3
	v_and_b32_e32 v216, 63, v0
	v_and_b32_e32 v217, 7, v216
	v_lshrrev_b32_e32 v216, 3, v216
	v_and_b32_e32 v218, 3, v217
	v_xor_b32_e32 v218, s12, v218
	v_lshlrev_b32_e32 v218, 5, v218
	v_lshl_add_u32 v218, v216, 2, v218
	v_lshl_add_u32 v218, v217, 9, v218
	v_and_b32_e32 v219, 0x1c0, v0
	v_lshl_add_u32 v218, v219, 6, v218
	v_add_u32_e32 v218, 0x1c000, v218
	ds_write_b32 v218, v212 offset:0
	ds_write_b32 v218, v213 offset:128
	ds_write_b32 v218, v214 offset:256
	ds_write_b32 v218, v215 offset:384
	s_mov_b32 s67, s25
	s_mov_b32 s25, 0

; __device__ __forceinline__ unsigned pk4_fp8(float a, float b, float c, float d) { int p = __builtin_amdgcn_cvt_pk_fp8_f32(a, b, 0, false); p = __builtin_amdgcn_cvt_pk_fp8_f32(c, d, p, true); return (unsigned)p; }
; __device__ __forceinline__ void witem_store(const WItem& w, const f32x4 (&v)[16]) {
;     if (!w.valid) return;
;     if (w.f8) {
; #pragma unroll
;         for (int j = 0; j < 4; ++j) { u32x4 o; const float sc = w.scale;
;             o.x = pk4_fp8(v[0][j] * sc, v[1][j] * sc, v[2][j] * sc, v[3][j] * sc); o.y = pk4_fp8(v[4][j] * sc, v[5][j] * sc, v[6][j] * sc, v[7][j] * sc);
;             o.z = pk4_fp8(v[8][j] * sc, v[9][j] * sc, v[10][j] * sc, v[11][j] * sc); o.w = pk4_fp8(v[12][j] * sc, v[13][j] * sc, v[14][j] * sc, v[15][j] * sc);
;             *(u32x4*)(w.dst + (size_t)witem_row(w.kind, w.n + j) * w.K + w.k0) = o; }
; __device__ __forceinline__ void p0_weights(const Args& a, LAS unsigned char* lds) {
;     ...
;         else if ((r -= I_FD) < 16 * I_MG) { const int up = r / (8 * I_MG); r -= up * 8 * I_MG; const int e = r / I_MG; r -= e * I_MG; W = a.in[up ? I_MWU : I_MWG] + (size_t)e * D * DFE; w.K = D; w.N = DFE;
;             w.dst = a.ws + WS_MGU_T + (size_t)e * 2 * DFE * D * (MOE_FP8 ? 1 : 2); w.kind = 2 + up; w.f8 = MOE_FP8; w.scale = F8_WGU; }
;         else { r -= 16 * I_MG; const int e = r / I_MD; r -= e * I_MD; W = a.in[I_MWD] + (size_t)e * DFE * D; w.K = DFE; w.N = D; w.dst = a.ws + WS_MD_T + (size_t)e * D * DFE * (MOE_FP8 ? 1 : 2); w.f8 = MOE_FP8; w.scale = F8_WD; }
.Lcn_wd_n1:
	s_bitcmp1_b32 s25, 31
	s_cbranch_scc0 .Lcn_snone_n1l
	s_and_b32 s14, s25, 0xfffffff
	s_lshr_b32 s14, s14, 2
	s_lshl_b32 s14, s14, 11
	s_add_u32 s14, s14, s100
	s_mov_b32 s15, 0x42000000
	s_cmp_ge_u32 s14, 0xe000
	s_cselect_b32 s15, 0x43000000, s15
	v_mul_f32_e32 v212, s15, v212
	v_mul_f32_e32 v213, s15, v213
	v_mul_f32_e32 v214, s15, v214
	v_mul_f32_e32 v215, s15, v215
	v_mul_f32_e32 v216, s15, v216
	v_mul_f32_e32 v217, s15, v217
	v_mul_f32_e32 v218, s15, v218
	v_mul_f32_e32 v219, s15, v219
	v_mul_f32_e32 v224, s15, v224
	v_mul_f32_e32 v225, s15, v225
	v_mul_f32_e32 v226, s15, v226
	v_mul_f32_e32 v227, s15, v227
	v_mul_f32_e32 v220, s15, v220
	v_mul_f32_e32 v221, s15, v221
	v_mul_f32_e32 v253, s15, v253
	v_mul_f32_e32 v254, s15, v254
	v_cvt_pk_fp8_f32 v212, v212, v216
	v_cvt_pk_fp8_f32 v213, v213, v217
	v_cvt_pk_fp8_f32 v214, v214, v218
	v_cvt_pk_fp8_f32 v215, v215, v219
	v_cvt_pk_fp8_f32 v212, v224, v220 op_sel:[0,0,1]
	v_cvt_pk_fp8_f32 v213, v225, v221 op_sel:[0,0,1]
	v_cvt_pk_fp8_f32 v214, v226, v253 op_sel:[0,0,1]
	v_cvt_pk_fp8_f32 v215, v227, v254 op_sel:[0,0,1]
	s_and_b32 s14, s25, 3
	v_and_b32_e32 v216, 63, v0
	v_and_b32_e32 v217, 7, v216
	v_lshrrev_b32_e32 v216, 3, v216
	v_and_b32_e32 v218, 3, v217
	v_xor_b32_e32 v218, s14, v218
	v_lshlrev_b32_e32 v218, 5, v218
	v_lshl_add_u32 v218, v216, 2, v218
	v_lshl_add_u32 v218, v217, 9, v218
	v_and_b32_e32 v219, 0x1c0, v0
	v_lshl_add_u32 v218, v219, 6, v218
	v_add_u32_e32 v218, 0x1c000, v218
	ds_write_b32 v218, v212 offset:0
	ds_write_b32 v218, v213 offset:128
	ds_write_b32 v218, v214 offset:256
	ds_write_b32 v218, v215 offset:384
	s_mov_b32 s67, s25
	s_mov_b32 s25, 0

; __device__ __forceinline__ unsigned pk4_fp8(float a, float b, float c, float d) { int p = __builtin_amdgcn_cvt_pk_fp8_f32(a, b, 0, false); p = __builtin_amdgcn_cvt_pk_fp8_f32(c, d, p, true); return (unsigned)p; }
; __device__ __forceinline__ void witem_store(const WItem& w, const f32x4 (&v)[16]) {
;     if (!w.valid) return;
;     if (w.f8) {
; #pragma unroll
;         for (int j = 0; j < 4; ++j) { u32x4 o; const float sc = w.scale;
;             o.x = pk4_fp8(v[0][j] * sc, v[1][j] * sc, v[2][j] * sc, v[3][j] * sc); o.y = pk4_fp8(v[4][j] * sc, v[5][j] * sc, v[6][j] * sc, v[7][j] * sc);
;             o.z = pk4_fp8(v[8][j] * sc, v[9][j] * sc, v[10][j] * sc, v[11][j] * sc); o.w = pk4_fp8(v[12][j] * sc, v[13][j] * sc, v[14][j] * sc, v[15][j] * sc);
;             *(u32x4*)(w.dst + (size_t)witem_row(w.kind, w.n + j) * w.K + w.k0) = o; }
; __device__ __forceinline__ void p0_weights(const Args& a, LAS unsigned char* lds) {
;     ...
;         else if ((r -= I_FD) < 16 * I_MG) { const int up = r / (8 * I_MG); r -= up * 8 * I_MG; const int e = r / I_MG; r -= e * I_MG; W = a.in[up ? I_MWU : I_MWG] + (size_t)e * D * DFE; w.K = D; w.N = DFE;
;             w.dst = a.ws + WS_MGU_T + (size_t)e * 2 * DFE * D * (MOE_FP8 ? 1 : 2); w.kind = 2 + up; w.f8 = MOE_FP8; w.scale = F8_WGU; }
;         else { r -= 16 * I_MG; const int e = r / I_MD; r -= e * I_MD; W = a.in[I_MWD] + (size_t)e * DFE * D; w.K = DFE; w.N = D; w.dst = a.ws + WS_MD_T + (size_t)e * D * DFE * (MOE_FP8 ? 1 : 2); w.f8 = MOE_FP8; w.scale = F8_WD; }
.Lcn_exit_n1:
	s_bitcmp1_b32 s25, 31
	s_cbranch_scc0 .Lcn_xnone_n1
	s_waitcnt vmcnt(0)
	s_bitcmp1_b32 s25, 31
	s_cbranch_scc0 .Lcn_snone_n1x
	s_and_b32 s14, s25, 0xfffffff
	s_lshr_b32 s14, s14, 2
	s_lshl_b32 s14, s14, 11
	s_add_u32 s14, s14, s100
	s_mov_b32 s15, 0x42000000
	s_cmp_ge_u32 s14, 0xe000
	s_cselect_b32 s15, 0x43000000, s15
	v_mul_f32_e32 v212, s15, v212
	v_mul_f32_e32 v213, s15, v213
	v_mul_f32_e32 v214, s15, v214
	v_mul_f32_e32 v215, s15, v215
	v_mul_f32_e32 v216, s15, v216
	v_mul_f32_e32 v217, s15, v217
	v_mul_f32_e32 v218, s15, v218
	v_mul_f32_e32 v219, s15, v219
	v_mul_f32_e32 v224, s15, v224
	v_mul_f32_e32 v225, s15, v225
	v_mul_f32_e32 v226, s15, v226
	v_mul_f32_e32 v227, s15, v227
	v_mul_f32_e32 v220, s15, v220
	v_mul_f32_e32 v221, s15, v221
	v_mul_f32_e32 v253, s15, v253
	v_mul_f32_e32 v254, s15, v254
	v_cvt_pk_fp8_f32 v212, v212, v216
	v_cvt_pk_fp8_f32 v213, v213, v217
	v_cvt_pk_fp8_f32 v214, v214, v218
	v_cvt_pk_fp8_f32 v215, v215, v219
	v_cvt_pk_fp8_f32 v212, v224, v220 op_sel:[0,0,1]
	v_cvt_pk_fp8_f32 v213, v225, v221 op_sel:[0,0,1]
	v_cvt_pk_fp8_f32 v214, v226, v253 op_sel:[0,0,1]
	v_cvt_pk_fp8_f32 v215, v227, v254 op_sel:[0,0,1]
	s_and_b32 s14, s25, 3
	v_and_b32_e32 v216, 63, v0
	v_and_b32_e32 v217, 7, v216
	v_lshrrev_b32_e32 v216, 3, v216
	v_and_b32_e32 v218, 3, v217
	v_xor_b32_e32 v218, s14, v218
	v_lshlrev_b32_e32 v218, 5, v218
	v_lshl_add_u32 v218, v216, 2, v218
	v_lshl_add_u32 v218, v217, 9, v218
	v_and_b32_e32 v219, 0x1c0, v0
	v_lshl_add_u32 v218, v219, 6, v218
	v_add_u32_e32 v218, 0x1c000, v218
	ds_write_b32 v218, v212 offset:0
	ds_write_b32 v218, v213 offset:128
	ds_write_b32 v218, v214 offset:256
	ds_write_b32 v218, v215 offset:384
	s_mov_b32 s67, s25
	s_mov_b32 s25, 0
